# workgroups idle in the last round of a MoE GEMM phase convert their own later lockstep items ahead of time (LDS marker, later barriers skip them)
# baseline (speedup 1.0000x reference)
.Lcvt_lock:
	s_cmp_ge_u32 s31, 12
	s_cbranch_scc0 .Lcvt_lk_n
	s_add_i32 s27, s62, 1
	s_sub_i32 s24, s31, 10
	s_cmp_ge_u32 s31, 16
	s_cbranch_scc0 .Lcvt_lk_c
	s_sub_i32 s24, s31, 11
	s_branch .Lcvt_lk_c
.Lcvt_lk_n:
	s_cmp_eq_u32 s31, 11
	s_cbranch_scc0 .Lcvt_lk_a
	s_mov_b32 s27, 0
	s_mov_b32 s24, 0
	v_mov_b32_e32 v11, 0x21dc0
	v_mov_b32_e32 v12, 0
	v_mov_b32_e32 v13, 0
	ds_write_b64 v11, v[12:13]
	s_waitcnt lgkmcnt(0)
	s_branch .Lcvt_lk_c

.Lcvt_lk_b:
	s_mov_b32 s24, -1
	s_cmp_eq_u32 s31, 0
	s_cselect_b32 s24, 0, s24
	s_cmp_eq_u32 s31, 1
	s_cselect_b32 s24, 1, s24
	s_cmp_eq_u32 s31, 2
	s_cselect_b32 s24, 2, s24
	s_cmp_eq_u32 s31, 4
	s_cselect_b32 s24, 3, s24
	s_cmp_eq_u32 s31, 6
	s_cselect_b32 s24, 4, s24
	s_cmp_eq_u32 s31, 7
	s_cselect_b32 s24, 5, s24
	s_cmp_lt_i32 s24, 0
	s_cbranch_scc1 .Lcvt_ret
	s_mov_b32 s27, s62
	s_cmp_eq_u32 s62, 0
	s_cselect_b32 s26, 1, 2
	s_add_i32 s24, s24, s26
	v_mov_b32_e32 v11, 0x21dc0
	ds_read_b64 v[12:13], v11
	s_add_i32 s5, s62, 1
	s_waitcnt lgkmcnt(0)
	v_readfirstlane_b32 s26, v12
	v_readfirstlane_b32 s4, v13
	s_cmp_eq_u32 s26, s5
	s_cbranch_scc0 .Lcvt_sk2
	s_cmp_ge_u32 s24, 2
	s_cbranch_scc0 .Lcvt_sk2
	s_cmp_le_u32 s24, 4
	s_cbranch_scc1 .Lcvt_ret
.Lcvt_sk2:
	s_cmp_eq_u32 s4, s5
	s_cbranch_scc0 .Lcvt_lk_c
	s_cmp_ge_u32 s24, 5
	s_cbranch_scc1 .Lcvt_ret

.Lcvt_ret:
	s_mov_b64 exec, -1
	s_cmp_lt_u32 s31, 12
	s_cbranch_scc1 .Lcvt_ret_a
	s_and_b32 s4, s31, 3
	s_cmp_eq_u32 s4, 2
	s_cbranch_scc1 .Lcvt_pre_done
	s_add_i32 s31, s31, 1
	v_readfirstlane_b32 s25, v2
	s_branch .Lcvt_lock
.Lcvt_pre_done:
	s_add_i32 s5, s62, 2
	v_mov_b32_e32 v11, 0x21dc0
	v_mov_b32_e32 v12, s5
	s_cmp_ge_u32 s31, 16
	s_cbranch_scc1 .Lcvt_pre_d10
	ds_write_b32 v11, v12
	s_waitcnt lgkmcnt(0)
	s_mov_b32 s31, 9
	s_branch .Lcvt_ret_b
.Lcvt_pre_d10:
	ds_write_b32 v11, v12 offset:4
	s_waitcnt lgkmcnt(0)
	s_mov_b32 s31, 10
	s_branch .Lcvt_ret_b
.Lcvt_ret_a:
	s_cmp_eq_u32 s31, 9
	s_cbranch_scc1 .Lcvt_idle
	s_cmp_eq_u32 s31, 10
	s_cbranch_scc0 .Lcvt_ret_b
	s_cmp_ge_u32 s63, 136
	s_cbranch_scc1 .Lcvt_ret_b
.Lcvt_idle:
	s_cmp_lg_u32 s92, 0x100
	s_cbranch_scc1 .Lcvt_ret_b
	s_cmp_ge_u32 s62, 3
	s_cbranch_scc1 .Lcvt_ret_b
	v_mov_b32_e32 v11, 0x20180
	ds_read_b32 v12, v11
	s_waitcnt lgkmcnt(0)
	v_readfirstlane_b32 s4, v12
	s_cmp_eq_u32 s31, 9
	s_cselect_b32 s5, 3, 2
	s_lshl_b32 s4, s4, s5
	s_add_i32 s4, s4, -1
	s_and_b32 s4, s4, 0xff
	s_add_i32 s4, s4, 1
	s_cmp_ge_u32 s63, s4
	s_cbranch_scc0 .Lcvt_ret_b
	s_cmp_eq_u32 s31, 9
	s_cselect_b32 s31, 12, 16
	v_readfirstlane_b32 s25, v2
	s_branch .Lcvt_lock
.Lcvt_ret_b:
	s_cmp_eq_u32 s31, 0
	s_cbranch_scc1 .LBB0_326
	s_cmp_eq_u32 s31, 1
	s_cbranch_scc1 .LBB0_404
	s_cmp_eq_u32 s31, 2
	s_cbranch_scc1 .LBB0_533
	s_cmp_eq_u32 s31, 3
	s_cbranch_scc1 .LBB0_610
	s_cmp_eq_u32 s31, 4
	s_cbranch_scc1 .LBB0_673
	s_cmp_eq_u32 s31, 5
	s_cbranch_scc1 .LBB0_849
	s_cmp_eq_u32 s31, 6
	s_cbranch_scc1 .LBB0_955
	s_cmp_eq_u32 s31, 7
	s_cbranch_scc1 .LBB0_1074
	s_cmp_eq_u32 s31, 8
	s_cbranch_scc1 .LBB0_1171
	s_cmp_eq_u32 s31, 9
	s_cbranch_scc1 .LBB0_1342
	s_cmp_eq_u32 s31, 10
	s_cbranch_scc1 .LBB0_245
	s_cmp_eq_u32 s31, 11
	s_cbranch_scc1 .LBB0_242
	s_branch .LBB0_326
